# GEMM mainloop rewritten: software-pipelined LDS fragment reads + 3-deep LDS-DMA prefetch, rolled loop
# speedup vs baseline: 1.0296x; 1.0296x over previous
_Z8gemm_qkvPKDF16_S0_PKfPDF16_S3_S3_Pj:
	v_readfirstlane_b32 s13, v0
	s_lshr_b32 s8, s13, 6
	v_bfe_u32 v2, v0, 3, 3
	s_load_dwordx4 s[4:7], s[0:1], 0x0
	v_lshl_or_b32 v6, s8, 3, v2
	v_lshrrev_b32_e32 v2, 1, v6
	s_mul_i32 s16, s3, 0xc0
	v_xor_b32_e32 v4, v2, v0
	v_add_u32_e32 v2, s16, v6
	v_ashrrev_i32_e32 v3, 31, v2
	s_bfe_u32 s15, s13, 0x20006
	v_lshlrev_b64 v[2:3], 11, v[2:3]
	v_lshlrev_b32_e32 v4, 4, v4
	s_mul_i32 s10, s2, 0xc0
	s_mul_i32 s2, s15, 48
	s_waitcnt lgkmcnt(0)
	v_lshl_add_u64 v[2:3], s[4:5], 0, v[2:3]
	v_and_b32_e32 v4, 0x70, v4
	v_mov_b32_e32 v5, 0
	s_add_i32 s17, s2, s10
	v_lshl_add_u64 v[218:219], v[2:3], 0, v[4:5]
	v_add_u32_e32 v2, s10, v6
	s_lshl_b32 s8, s8, 10
	v_ashrrev_i32_e32 v3, 31, v2
	s_cmp_lg_u32 0x400, -1
	v_lshlrev_b64 v[2:3], 11, v[2:3]
	s_cselect_b32 s4, 0x400, 0
	v_lshl_add_u64 v[2:3], s[6:7], 0, v[2:3]
	s_add_i32 s11, s8, s4
	s_mov_b32 s4, m0
	s_mov_b32 m0, s11
	s_nop 0
	global_load_lds_dwordx4 v[218:219], off
	s_mov_b32 m0, s4
	v_lshl_add_u64 v[220:221], v[2:3], 0, v[4:5]
	s_add_i32 s4, s11, 0x6000
	s_mov_b32 s5, m0
	s_mov_b32 m0, s4
	s_nop 0
	global_load_lds_dwordx4 v[220:221], off
	s_mov_b32 m0, s5
	s_mov_b64 s[4:5], 0x20000
	v_lshl_add_u64 v[222:223], v[218:219], 0, s[4:5]
	s_add_i32 s9, s11, 0x2000
	s_mov_b32 s6, m0
	s_mov_b32 m0, s9
	s_nop 0
	global_load_lds_dwordx4 v[222:223], off
	s_mov_b32 m0, s6
	v_lshl_add_u64 v[224:225], v[220:221], 0, s[4:5]
	s_add_i32 s4, s11, 0x8000
	s_mov_b32 s5, m0
	s_mov_b32 m0, s4
	s_nop 0
	global_load_lds_dwordx4 v[224:225], off
	s_mov_b32 m0, s5
	s_mov_b64 s[4:5], 0x40000
	v_lshl_add_u64 v[226:227], v[218:219], 0, s[4:5]
	s_add_i32 s12, s11, 0x4000
	s_mov_b32 s6, m0
	s_mov_b32 m0, s12
	s_nop 0
	global_load_lds_dwordx4 v[226:227], off
	s_mov_b32 m0, s6
	v_lshl_add_u64 v[228:229], v[220:221], 0, s[4:5]
	s_add_i32 s4, s11, 0xa000
	s_mov_b32 s5, m0
	s_mov_b32 m0, s4
	s_nop 0
	global_load_lds_dwordx4 v[228:229], off
	s_mov_b32 m0, s5
	s_cmpk_gt_i32 s17, 0x7d0
	s_cselect_b64 s[4:5], -1, 0
	s_lshr_b32 s14, s13, 8
	s_mul_i32 s6, s14, 0x3000
	s_add_i32 s13, s6, 0x400
	s_mov_b64 s[6:7], 0x80
	s_add_i32 s18, s11, 0xc000
	v_lshl_add_u64 v[2:3], v[218:219], 0, s[6:7]
	s_mov_b32 s30, m0
	s_mov_b32 m0, s18
	s_nop 0
	global_load_lds_dwordx4 v[2:3], off
	s_mov_b32 m0, s30
	s_add_i32 s19, s11, 0x12000
	v_lshl_add_u64 v[2:3], v[220:221], 0, s[6:7]
	s_mov_b32 s6, m0
	s_mov_b32 m0, s19
	s_nop 0
	global_load_lds_dwordx4 v[2:3], off
	s_mov_b32 m0, s6
	s_mov_b64 s[6:7], 0x20080
	s_add_i32 s20, s11, 0xe000
	v_lshl_add_u64 v[2:3], v[218:219], 0, s[6:7]
	s_mov_b32 s18, m0
	s_mov_b32 m0, s20
	s_nop 0
	global_load_lds_dwordx4 v[2:3], off
	s_mov_b32 m0, s18
	s_add_i32 s21, s11, 0x14000
	v_lshl_add_u64 v[2:3], v[220:221], 0, s[6:7]
	s_mov_b32 s6, m0
	s_mov_b32 m0, s21
	s_nop 0
	global_load_lds_dwordx4 v[2:3], off
	s_mov_b32 m0, s6
	s_mov_b64 s[6:7], 0x40080
	v_lshl_add_u64 v[2:3], v[218:219], 0, s[6:7]
	s_add_i32 s22, s11, 0x10000
	s_mov_b32 s18, m0
	s_mov_b32 m0, s22
	s_nop 0
	global_load_lds_dwordx4 v[2:3], off
	s_mov_b32 m0, s18
	v_lshl_add_u64 v[2:3], v[220:221], 0, s[6:7]
	v_and_b32_e32 v1, 15, v0
	v_bfe_u32 v231, v0, 4, 2
	s_add_i32 s23, s11, 0x16000
	s_mov_b32 s6, m0
	s_mov_b32 m0, s23
	s_nop 0
	global_load_lds_dwordx4 v[2:3], off
	s_mov_b32 m0, s6
	v_lshrrev_b32_e32 v3, 1, v0
	v_lshlrev_b32_e32 v2, 7, v1
	v_bfe_u32 v4, v0, 1, 3
	v_bitop3_b32 v3, v231, v3, 7 bitop3:0x78
	v_lshl_or_b32 v238, v3, 4, v2
	v_bitop3_b32 v3, v231, v4, 4 bitop3:0x36
	v_lshl_or_b32 v240, v3, 4, v2
	s_mulk_i32 s15, 0x1800
	s_addk_i32 s15, 0x6400
	v_add_u32_e32 v158, s13, v238
	v_add_u32_e32 v160, s13, v240
	v_add_u32_e32 v162, s15, v238
	v_add_u32_e32 v164, s15, v240
	s_add_u32 m0, s11, 0x17f00
	s_nop 0
	global_load_lds_dwordx4 v[218:219], off offset:256
	s_add_u32 m0, s11, 0x1df00
	s_nop 0
	global_load_lds_dwordx4 v[220:221], off offset:256
	s_add_u32 m0, s11, 0x19f00
	s_nop 0
	global_load_lds_dwordx4 v[222:223], off offset:256
	s_add_u32 m0, s11, 0x1ff00
	s_nop 0
	global_load_lds_dwordx4 v[224:225], off offset:256
	s_add_u32 m0, s11, 0x1bf00
	s_nop 0
	global_load_lds_dwordx4 v[226:227], off offset:256
	s_add_u32 m0, s11, 0x21f00
	s_nop 0
	global_load_lds_dwordx4 v[228:229], off offset:256
	s_load_dwordx2 s[24:25], s[0:1], 0x10
	s_mov_b32 s20, 0x180
	s_mov_b32 s21, 0
	v_lshl_add_u64 v[218:219], v[218:219], 0, s[20:21]
	v_lshl_add_u64 v[222:223], v[222:223], 0, s[20:21]
	v_lshl_add_u64 v[226:227], v[226:227], 0, s[20:21]
	v_lshl_add_u64 v[220:221], v[220:221], 0, s[20:21]
	v_lshl_add_u64 v[224:225], v[224:225], 0, s[20:21]
	v_lshl_add_u64 v[228:229], v[228:229], 0, s[20:21]
	v_add_u32_e32 v159, 0x18000, v158
	v_add_u32_e32 v161, 0x18000, v160
	v_add_u32_e32 v163, 0x18000, v162
	v_add_u32_e32 v165, 0x18000, v164
	v_mov_b32_e32 v82, 0
	v_mov_b32_e32 v83, 0
	v_mov_b32_e32 v84, 0
	v_mov_b32_e32 v85, 0
	v_mov_b32_e32 v58, 0
	v_mov_b32_e32 v59, 0
	v_mov_b32_e32 v60, 0
	v_mov_b32_e32 v61, 0
	v_mov_b32_e32 v14, 0
	v_mov_b32_e32 v15, 0
	v_mov_b32_e32 v16, 0
	v_mov_b32_e32 v17, 0
	v_mov_b32_e32 v78, 0
	v_mov_b32_e32 v79, 0
	v_mov_b32_e32 v80, 0
	v_mov_b32_e32 v81, 0
	v_mov_b32_e32 v22, 0
	v_mov_b32_e32 v23, 0
	v_mov_b32_e32 v24, 0
	v_mov_b32_e32 v25, 0
	v_mov_b32_e32 v30, 0
	v_mov_b32_e32 v31, 0
	v_mov_b32_e32 v32, 0
	v_mov_b32_e32 v33, 0
	v_mov_b32_e32 v74, 0
	v_mov_b32_e32 v75, 0
	v_mov_b32_e32 v76, 0
	v_mov_b32_e32 v77, 0
	v_mov_b32_e32 v18, 0
	v_mov_b32_e32 v19, 0
	v_mov_b32_e32 v20, 0
	v_mov_b32_e32 v21, 0
	v_mov_b32_e32 v26, 0
	v_mov_b32_e32 v27, 0
	v_mov_b32_e32 v28, 0
	v_mov_b32_e32 v29, 0
	v_mov_b32_e32 v70, 0
	v_mov_b32_e32 v71, 0
	v_mov_b32_e32 v72, 0
	v_mov_b32_e32 v73, 0
	v_mov_b32_e32 v46, 0
	v_mov_b32_e32 v47, 0
	v_mov_b32_e32 v48, 0
	v_mov_b32_e32 v49, 0
	v_mov_b32_e32 v240, 0
	v_mov_b32_e32 v241, 0
	v_mov_b32_e32 v242, 0
	v_mov_b32_e32 v243, 0
	v_mov_b32_e32 v66, 0
	v_mov_b32_e32 v67, 0
	v_mov_b32_e32 v68, 0
	v_mov_b32_e32 v69, 0
	v_mov_b32_e32 v42, 0
	v_mov_b32_e32 v43, 0
	v_mov_b32_e32 v44, 0
	v_mov_b32_e32 v45, 0
	v_mov_b32_e32 v236, 0
	v_mov_b32_e32 v237, 0
	v_mov_b32_e32 v238, 0
	v_mov_b32_e32 v239, 0
	v_mov_b32_e32 v62, 0
	v_mov_b32_e32 v63, 0
	v_mov_b32_e32 v64, 0
	v_mov_b32_e32 v65, 0
	v_mov_b32_e32 v38, 0
	v_mov_b32_e32 v39, 0
	v_mov_b32_e32 v40, 0
	v_mov_b32_e32 v41, 0
	v_mov_b32_e32 v34, 0
	v_mov_b32_e32 v35, 0
	v_mov_b32_e32 v36, 0
	v_mov_b32_e32 v37, 0
	s_not_b64 s[6:7], s[4:5]
	s_mov_b32 s22, 4
	s_waitcnt vmcnt(12) lgkmcnt(0)
	s_barrier
	ds_read_b128 v[134:137], v162
	ds_read_b128 v[138:141], v162 offset:2048
	ds_read_b128 v[142:145], v162 offset:4096
	ds_read_b128 v[86:89], v158
	ds_read_b128 v[90:93], v158 offset:2048
	ds_read_b128 v[94:97], v158 offset:4096
	ds_read_b128 v[98:101], v158 offset:6144
	ds_read_b128 v[102:105], v158 offset:8192
	ds_read_b128 v[106:109], v158 offset:10240
	ds_read_b128 v[110:113], v160
	ds_read_b128 v[114:117], v160 offset:2048
	ds_read_b128 v[118:121], v160 offset:4096
	ds_read_b128 v[122:125], v160 offset:6144
	ds_read_b128 v[126:129], v160 offset:8192
	ds_read_b128 v[130:133], v160 offset:10240
	ds_read_b128 v[146:149], v164
	ds_read_b128 v[150:153], v164 offset:2048
	ds_read_b128 v[154:157], v164 offset:4096
	s_and_b64 vcc, exec, s[4:5]
	s_cbranch_vccnz .Lgemm_N_loop
.Lgemm_T_loop:
	s_waitcnt lgkmcnt(9)
	v_mfma_f32_16x16x32_f16 v[82:85], v[134:137], v[86:89], v[82:85]
	v_mfma_f32_16x16x32_f16 v[58:61], v[138:141], v[86:89], v[58:61]
	v_mfma_f32_16x16x32_f16 v[14:17], v[142:145], v[86:89], v[14:17]
	v_mfma_f32_16x16x32_f16 v[78:81], v[134:137], v[90:93], v[78:81]
	v_mfma_f32_16x16x32_f16 v[22:25], v[138:141], v[90:93], v[22:25]
	v_mfma_f32_16x16x32_f16 v[30:33], v[142:145], v[90:93], v[30:33]
	v_mfma_f32_16x16x32_f16 v[74:77], v[134:137], v[94:97], v[74:77]
	v_mfma_f32_16x16x32_f16 v[18:21], v[138:141], v[94:97], v[18:21]
	v_mfma_f32_16x16x32_f16 v[26:29], v[142:145], v[94:97], v[26:29]
	v_mfma_f32_16x16x32_f16 v[70:73], v[134:137], v[98:101], v[70:73]
	v_mfma_f32_16x16x32_f16 v[46:49], v[138:141], v[98:101], v[46:49]
	v_mfma_f32_16x16x32_f16 v[240:243], v[142:145], v[98:101], v[240:243]
	v_mfma_f32_16x16x32_f16 v[66:69], v[134:137], v[102:105], v[66:69]
	v_mfma_f32_16x16x32_f16 v[42:45], v[138:141], v[102:105], v[42:45]
	v_mfma_f32_16x16x32_f16 v[236:239], v[142:145], v[102:105], v[236:239]
	v_mfma_f32_16x16x32_f16 v[62:65], v[134:137], v[106:109], v[62:65]
	v_mfma_f32_16x16x32_f16 v[38:41], v[138:141], v[106:109], v[38:41]
	v_mfma_f32_16x16x32_f16 v[34:37], v[142:145], v[106:109], v[34:37]
	s_waitcnt vmcnt(6) lgkmcnt(0)
	s_barrier
	s_add_u32 m0, s11, 0x0
	ds_read_b128 v[134:137], v162 offset:49152
	global_load_lds_dwordx4 v[218:219], off
	v_mfma_f32_16x16x32_f16 v[82:85], v[146:149], v[110:113], v[82:85]
	s_add_u32 m0, s11, 0x6000
	ds_read_b128 v[138:141], v162 offset:51200
	global_load_lds_dwordx4 v[220:221], off
	v_mfma_f32_16x16x32_f16 v[58:61], v[150:153], v[110:113], v[58:61]
	s_add_u32 m0, s11, 0x2000
	ds_read_b128 v[142:145], v162 offset:53248
	global_load_lds_dwordx4 v[222:223], off
	v_mfma_f32_16x16x32_f16 v[14:17], v[154:157], v[110:113], v[14:17]
	s_add_u32 m0, s11, 0x8000
	ds_read_b128 v[86:89], v158 offset:49152
	global_load_lds_dwordx4 v[224:225], off
	v_mfma_f32_16x16x32_f16 v[78:81], v[146:149], v[114:117], v[78:81]
	s_add_u32 m0, s11, 0x4000
	ds_read_b128 v[90:93], v158 offset:51200
	global_load_lds_dwordx4 v[226:227], off
	v_mfma_f32_16x16x32_f16 v[22:25], v[150:153], v[114:117], v[22:25]
	s_add_u32 m0, s11, 0xa000
	ds_read_b128 v[94:97], v158 offset:53248
	global_load_lds_dwordx4 v[228:229], off
	v_mfma_f32_16x16x32_f16 v[30:33], v[154:157], v[114:117], v[30:33]
	ds_read_b128 v[98:101], v158 offset:55296
	v_mfma_f32_16x16x32_f16 v[74:77], v[146:149], v[118:121], v[74:77]
	ds_read_b128 v[102:105], v158 offset:57344
	v_mfma_f32_16x16x32_f16 v[18:21], v[150:153], v[118:121], v[18:21]
	ds_read_b128 v[106:109], v158 offset:59392
	v_mfma_f32_16x16x32_f16 v[26:29], v[154:157], v[118:121], v[26:29]
	ds_read_b128 v[110:113], v160 offset:49152
	v_mfma_f32_16x16x32_f16 v[70:73], v[146:149], v[122:125], v[70:73]
	ds_read_b128 v[114:117], v160 offset:51200
	v_mfma_f32_16x16x32_f16 v[46:49], v[150:153], v[122:125], v[46:49]
	v_mfma_f32_16x16x32_f16 v[240:243], v[154:157], v[122:125], v[240:243]
	ds_read_b128 v[118:121], v160 offset:53248
	v_mfma_f32_16x16x32_f16 v[66:69], v[146:149], v[126:129], v[66:69]
	ds_read_b128 v[122:125], v160 offset:55296
	v_mfma_f32_16x16x32_f16 v[42:45], v[150:153], v[126:129], v[42:45]
	v_mfma_f32_16x16x32_f16 v[236:239], v[154:157], v[126:129], v[236:239]
	ds_read_b128 v[126:129], v160 offset:57344
	v_mfma_f32_16x16x32_f16 v[62:65], v[146:149], v[130:133], v[62:65]
	v_mfma_f32_16x16x32_f16 v[38:41], v[150:153], v[130:133], v[38:41]
	v_mfma_f32_16x16x32_f16 v[34:37], v[154:157], v[130:133], v[34:37]
	ds_read_b128 v[130:133], v160 offset:59392
	ds_read_b128 v[146:149], v164 offset:49152
	ds_read_b128 v[150:153], v164 offset:51200
	ds_read_b128 v[154:157], v164 offset:53248
	s_waitcnt lgkmcnt(9)
	v_mfma_f32_16x16x32_f16 v[82:85], v[134:137], v[86:89], v[82:85]
	v_mfma_f32_16x16x32_f16 v[58:61], v[138:141], v[86:89], v[58:61]
	v_mfma_f32_16x16x32_f16 v[14:17], v[142:145], v[86:89], v[14:17]
	v_mfma_f32_16x16x32_f16 v[78:81], v[134:137], v[90:93], v[78:81]
	v_mfma_f32_16x16x32_f16 v[22:25], v[138:141], v[90:93], v[22:25]
	v_mfma_f32_16x16x32_f16 v[30:33], v[142:145], v[90:93], v[30:33]
	v_mfma_f32_16x16x32_f16 v[74:77], v[134:137], v[94:97], v[74:77]
	v_mfma_f32_16x16x32_f16 v[18:21], v[138:141], v[94:97], v[18:21]
	v_mfma_f32_16x16x32_f16 v[26:29], v[142:145], v[94:97], v[26:29]
	v_mfma_f32_16x16x32_f16 v[70:73], v[134:137], v[98:101], v[70:73]
	v_mfma_f32_16x16x32_f16 v[46:49], v[138:141], v[98:101], v[46:49]
	v_mfma_f32_16x16x32_f16 v[240:243], v[142:145], v[98:101], v[240:243]
	v_mfma_f32_16x16x32_f16 v[66:69], v[134:137], v[102:105], v[66:69]
	v_mfma_f32_16x16x32_f16 v[42:45], v[138:141], v[102:105], v[42:45]
	v_mfma_f32_16x16x32_f16 v[236:239], v[142:145], v[102:105], v[236:239]
	v_mfma_f32_16x16x32_f16 v[62:65], v[134:137], v[106:109], v[62:65]
	v_mfma_f32_16x16x32_f16 v[38:41], v[138:141], v[106:109], v[38:41]
	v_mfma_f32_16x16x32_f16 v[34:37], v[142:145], v[106:109], v[34:37]
	s_waitcnt vmcnt(6) lgkmcnt(0)
	s_barrier
	s_add_u32 m0, s11, 0xbf80
	ds_read_b128 v[134:137], v163
	global_load_lds_dwordx4 v[218:219], off offset:128
	v_mfma_f32_16x16x32_f16 v[82:85], v[146:149], v[110:113], v[82:85]
	s_add_u32 m0, s11, 0x11f80
	ds_read_b128 v[138:141], v163 offset:2048
	global_load_lds_dwordx4 v[220:221], off offset:128
	v_mfma_f32_16x16x32_f16 v[58:61], v[150:153], v[110:113], v[58:61]
	s_add_u32 m0, s11, 0xdf80
	ds_read_b128 v[142:145], v163 offset:4096
	global_load_lds_dwordx4 v[222:223], off offset:128
	v_mfma_f32_16x16x32_f16 v[14:17], v[154:157], v[110:113], v[14:17]
	s_add_u32 m0, s11, 0x13f80
	ds_read_b128 v[86:89], v159
	global_load_lds_dwordx4 v[224:225], off offset:128
	v_mfma_f32_16x16x32_f16 v[78:81], v[146:149], v[114:117], v[78:81]
	s_add_u32 m0, s11, 0xff80
	ds_read_b128 v[90:93], v159 offset:2048
	global_load_lds_dwordx4 v[226:227], off offset:128
	v_mfma_f32_16x16x32_f16 v[22:25], v[150:153], v[114:117], v[22:25]
	s_add_u32 m0, s11, 0x15f80
	ds_read_b128 v[94:97], v159 offset:4096
	global_load_lds_dwordx4 v[228:229], off offset:128
	v_mfma_f32_16x16x32_f16 v[30:33], v[154:157], v[114:117], v[30:33]
	ds_read_b128 v[98:101], v159 offset:6144
	v_mfma_f32_16x16x32_f16 v[74:77], v[146:149], v[118:121], v[74:77]
	ds_read_b128 v[102:105], v159 offset:8192
	v_mfma_f32_16x16x32_f16 v[18:21], v[150:153], v[118:121], v[18:21]
	ds_read_b128 v[106:109], v159 offset:10240
	v_mfma_f32_16x16x32_f16 v[26:29], v[154:157], v[118:121], v[26:29]
	ds_read_b128 v[110:113], v161
	v_mfma_f32_16x16x32_f16 v[70:73], v[146:149], v[122:125], v[70:73]
	ds_read_b128 v[114:117], v161 offset:2048
	v_mfma_f32_16x16x32_f16 v[46:49], v[150:153], v[122:125], v[46:49]
	v_mfma_f32_16x16x32_f16 v[240:243], v[154:157], v[122:125], v[240:243]
	ds_read_b128 v[118:121], v161 offset:4096
	v_mfma_f32_16x16x32_f16 v[66:69], v[146:149], v[126:129], v[66:69]
	ds_read_b128 v[122:125], v161 offset:6144
	v_mfma_f32_16x16x32_f16 v[42:45], v[150:153], v[126:129], v[42:45]
	v_mfma_f32_16x16x32_f16 v[236:239], v[154:157], v[126:129], v[236:239]
	ds_read_b128 v[126:129], v161 offset:8192
	v_mfma_f32_16x16x32_f16 v[62:65], v[146:149], v[130:133], v[62:65]
	v_mfma_f32_16x16x32_f16 v[38:41], v[150:153], v[130:133], v[38:41]
	v_mfma_f32_16x16x32_f16 v[34:37], v[154:157], v[130:133], v[34:37]
	ds_read_b128 v[130:133], v161 offset:10240
	ds_read_b128 v[146:149], v165
	ds_read_b128 v[150:153], v165 offset:2048
	ds_read_b128 v[154:157], v165 offset:4096
	s_waitcnt lgkmcnt(9)
	v_mfma_f32_16x16x32_f16 v[82:85], v[134:137], v[86:89], v[82:85]
	v_mfma_f32_16x16x32_f16 v[58:61], v[138:141], v[86:89], v[58:61]
	v_mfma_f32_16x16x32_f16 v[14:17], v[142:145], v[86:89], v[14:17]
	v_mfma_f32_16x16x32_f16 v[78:81], v[134:137], v[90:93], v[78:81]
	v_mfma_f32_16x16x32_f16 v[22:25], v[138:141], v[90:93], v[22:25]
	v_mfma_f32_16x16x32_f16 v[30:33], v[142:145], v[90:93], v[30:33]
	v_mfma_f32_16x16x32_f16 v[74:77], v[134:137], v[94:97], v[74:77]
	v_mfma_f32_16x16x32_f16 v[18:21], v[138:141], v[94:97], v[18:21]
	v_mfma_f32_16x16x32_f16 v[26:29], v[142:145], v[94:97], v[26:29]
	v_mfma_f32_16x16x32_f16 v[70:73], v[134:137], v[98:101], v[70:73]
	v_mfma_f32_16x16x32_f16 v[46:49], v[138:141], v[98:101], v[46:49]
	v_mfma_f32_16x16x32_f16 v[240:243], v[142:145], v[98:101], v[240:243]
	v_mfma_f32_16x16x32_f16 v[66:69], v[134:137], v[102:105], v[66:69]
	v_mfma_f32_16x16x32_f16 v[42:45], v[138:141], v[102:105], v[42:45]
	v_mfma_f32_16x16x32_f16 v[236:239], v[142:145], v[102:105], v[236:239]
	v_mfma_f32_16x16x32_f16 v[62:65], v[134:137], v[106:109], v[62:65]
	v_mfma_f32_16x16x32_f16 v[38:41], v[138:141], v[106:109], v[38:41]
	v_mfma_f32_16x16x32_f16 v[34:37], v[142:145], v[106:109], v[34:37]
	s_waitcnt vmcnt(6) lgkmcnt(0)
	s_barrier
	s_add_u32 m0, s11, 0x17f00
	ds_read_b128 v[134:137], v162
	global_load_lds_dwordx4 v[218:219], off offset:256
	v_mfma_f32_16x16x32_f16 v[82:85], v[146:149], v[110:113], v[82:85]
	s_add_u32 m0, s11, 0x1df00
	ds_read_b128 v[138:141], v162 offset:2048
	global_load_lds_dwordx4 v[220:221], off offset:256
	v_mfma_f32_16x16x32_f16 v[58:61], v[150:153], v[110:113], v[58:61]
	s_add_u32 m0, s11, 0x19f00
	ds_read_b128 v[142:145], v162 offset:4096
	global_load_lds_dwordx4 v[222:223], off offset:256
	v_mfma_f32_16x16x32_f16 v[14:17], v[154:157], v[110:113], v[14:17]
	s_add_u32 m0, s11, 0x1ff00
	ds_read_b128 v[86:89], v158
	global_load_lds_dwordx4 v[224:225], off offset:256
	v_mfma_f32_16x16x32_f16 v[78:81], v[146:149], v[114:117], v[78:81]
	s_add_u32 m0, s11, 0x1bf00
	ds_read_b128 v[90:93], v158 offset:2048
	global_load_lds_dwordx4 v[226:227], off offset:256
	v_mfma_f32_16x16x32_f16 v[22:25], v[150:153], v[114:117], v[22:25]
	s_add_u32 m0, s11, 0x21f00
	ds_read_b128 v[94:97], v158 offset:4096
	global_load_lds_dwordx4 v[228:229], off offset:256
	v_mfma_f32_16x16x32_f16 v[30:33], v[154:157], v[114:117], v[30:33]
	ds_read_b128 v[98:101], v158 offset:6144
	v_mfma_f32_16x16x32_f16 v[74:77], v[146:149], v[118:121], v[74:77]
	ds_read_b128 v[102:105], v158 offset:8192
	v_mfma_f32_16x16x32_f16 v[18:21], v[150:153], v[118:121], v[18:21]
	ds_read_b128 v[106:109], v158 offset:10240
	v_mfma_f32_16x16x32_f16 v[26:29], v[154:157], v[118:121], v[26:29]
	ds_read_b128 v[110:113], v160
	v_mfma_f32_16x16x32_f16 v[70:73], v[146:149], v[122:125], v[70:73]
	ds_read_b128 v[114:117], v160 offset:2048
	v_mfma_f32_16x16x32_f16 v[46:49], v[150:153], v[122:125], v[46:49]
	v_mfma_f32_16x16x32_f16 v[240:243], v[154:157], v[122:125], v[240:243]
	ds_read_b128 v[118:121], v160 offset:4096
	v_mfma_f32_16x16x32_f16 v[66:69], v[146:149], v[126:129], v[66:69]
	ds_read_b128 v[122:125], v160 offset:6144
	v_mfma_f32_16x16x32_f16 v[42:45], v[150:153], v[126:129], v[42:45]
	v_mfma_f32_16x16x32_f16 v[236:239], v[154:157], v[126:129], v[236:239]
	ds_read_b128 v[126:129], v160 offset:8192
	v_mfma_f32_16x16x32_f16 v[62:65], v[146:149], v[130:133], v[62:65]
	v_mfma_f32_16x16x32_f16 v[38:41], v[150:153], v[130:133], v[38:41]
	v_mfma_f32_16x16x32_f16 v[34:37], v[154:157], v[130:133], v[34:37]
	ds_read_b128 v[130:133], v160 offset:10240
	ds_read_b128 v[146:149], v164
	ds_read_b128 v[150:153], v164 offset:2048
	ds_read_b128 v[154:157], v164 offset:4096
	v_lshl_add_u64 v[218:219], v[218:219], 0, s[20:21]
	v_lshl_add_u64 v[222:223], v[222:223], 0, s[20:21]
	v_lshl_add_u64 v[226:227], v[226:227], 0, s[20:21]
	v_lshl_add_u64 v[220:221], v[220:221], 0, s[20:21]
	v_lshl_add_u64 v[224:225], v[224:225], 0, s[20:21]
	v_lshl_add_u64 v[228:229], v[228:229], 0, s[20:21]
	s_sub_u32 s22, s22, 1
	s_cmp_lg_u32 s22, 0
	s_cbranch_scc1 .Lgemm_T_loop
	s_waitcnt lgkmcnt(9)
	v_mfma_f32_16x16x32_f16 v[82:85], v[134:137], v[86:89], v[82:85]
	v_mfma_f32_16x16x32_f16 v[58:61], v[138:141], v[86:89], v[58:61]
	v_mfma_f32_16x16x32_f16 v[14:17], v[142:145], v[86:89], v[14:17]
	v_mfma_f32_16x16x32_f16 v[78:81], v[134:137], v[90:93], v[78:81]
	v_mfma_f32_16x16x32_f16 v[22:25], v[138:141], v[90:93], v[22:25]
	v_mfma_f32_16x16x32_f16 v[30:33], v[142:145], v[90:93], v[30:33]
	v_mfma_f32_16x16x32_f16 v[74:77], v[134:137], v[94:97], v[74:77]
	v_mfma_f32_16x16x32_f16 v[18:21], v[138:141], v[94:97], v[18:21]
	v_mfma_f32_16x16x32_f16 v[26:29], v[142:145], v[94:97], v[26:29]
	v_mfma_f32_16x16x32_f16 v[70:73], v[134:137], v[98:101], v[70:73]
	v_mfma_f32_16x16x32_f16 v[46:49], v[138:141], v[98:101], v[46:49]
	v_mfma_f32_16x16x32_f16 v[240:243], v[142:145], v[98:101], v[240:243]
	v_mfma_f32_16x16x32_f16 v[66:69], v[134:137], v[102:105], v[66:69]
	v_mfma_f32_16x16x32_f16 v[42:45], v[138:141], v[102:105], v[42:45]
	v_mfma_f32_16x16x32_f16 v[236:239], v[142:145], v[102:105], v[236:239]
	v_mfma_f32_16x16x32_f16 v[62:65], v[134:137], v[106:109], v[62:65]
	v_mfma_f32_16x16x32_f16 v[38:41], v[138:141], v[106:109], v[38:41]
	v_mfma_f32_16x16x32_f16 v[34:37], v[142:145], v[106:109], v[34:37]
	s_waitcnt vmcnt(6) lgkmcnt(0)
	s_barrier
	s_add_u32 m0, s11, 0x0
	ds_read_b128 v[134:137], v162 offset:49152
	global_load_lds_dwordx4 v[218:219], off
	v_mfma_f32_16x16x32_f16 v[82:85], v[146:149], v[110:113], v[82:85]
	s_add_u32 m0, s11, 0x6000
	ds_read_b128 v[138:141], v162 offset:51200
	global_load_lds_dwordx4 v[220:221], off
	v_mfma_f32_16x16x32_f16 v[58:61], v[150:153], v[110:113], v[58:61]
	s_add_u32 m0, s11, 0x2000
	ds_read_b128 v[142:145], v162 offset:53248
	global_load_lds_dwordx4 v[222:223], off
	v_mfma_f32_16x16x32_f16 v[14:17], v[154:157], v[110:113], v[14:17]
	s_add_u32 m0, s11, 0x8000
	ds_read_b128 v[86:89], v158 offset:49152
	global_load_lds_dwordx4 v[224:225], off
	v_mfma_f32_16x16x32_f16 v[78:81], v[146:149], v[114:117], v[78:81]
	s_add_u32 m0, s11, 0x4000
	ds_read_b128 v[90:93], v158 offset:51200
	global_load_lds_dwordx4 v[226:227], off
	v_mfma_f32_16x16x32_f16 v[22:25], v[150:153], v[114:117], v[22:25]
	s_add_u32 m0, s11, 0xa000
	ds_read_b128 v[94:97], v158 offset:53248
	global_load_lds_dwordx4 v[228:229], off
	v_mfma_f32_16x16x32_f16 v[30:33], v[154:157], v[114:117], v[30:33]
	ds_read_b128 v[98:101], v158 offset:55296
	v_mfma_f32_16x16x32_f16 v[74:77], v[146:149], v[118:121], v[74:77]
	ds_read_b128 v[102:105], v158 offset:57344
	v_mfma_f32_16x16x32_f16 v[18:21], v[150:153], v[118:121], v[18:21]
	ds_read_b128 v[106:109], v158 offset:59392
	v_mfma_f32_16x16x32_f16 v[26:29], v[154:157], v[118:121], v[26:29]
	ds_read_b128 v[110:113], v160 offset:49152
	v_mfma_f32_16x16x32_f16 v[70:73], v[146:149], v[122:125], v[70:73]
	ds_read_b128 v[114:117], v160 offset:51200
	v_mfma_f32_16x16x32_f16 v[46:49], v[150:153], v[122:125], v[46:49]
	v_mfma_f32_16x16x32_f16 v[240:243], v[154:157], v[122:125], v[240:243]
	ds_read_b128 v[118:121], v160 offset:53248
	v_mfma_f32_16x16x32_f16 v[66:69], v[146:149], v[126:129], v[66:69]
	ds_read_b128 v[122:125], v160 offset:55296
	v_mfma_f32_16x16x32_f16 v[42:45], v[150:153], v[126:129], v[42:45]
	v_mfma_f32_16x16x32_f16 v[236:239], v[154:157], v[126:129], v[236:239]
	ds_read_b128 v[126:129], v160 offset:57344
	v_mfma_f32_16x16x32_f16 v[62:65], v[146:149], v[130:133], v[62:65]
	v_mfma_f32_16x16x32_f16 v[38:41], v[150:153], v[130:133], v[38:41]
	v_mfma_f32_16x16x32_f16 v[34:37], v[154:157], v[130:133], v[34:37]
	ds_read_b128 v[130:133], v160 offset:59392
	ds_read_b128 v[146:149], v164 offset:49152
	ds_read_b128 v[150:153], v164 offset:51200
	ds_read_b128 v[154:157], v164 offset:53248
	s_waitcnt lgkmcnt(9)
	v_mfma_f32_16x16x32_f16 v[82:85], v[134:137], v[86:89], v[82:85]
	v_mfma_f32_16x16x32_f16 v[58:61], v[138:141], v[86:89], v[58:61]
	v_mfma_f32_16x16x32_f16 v[14:17], v[142:145], v[86:89], v[14:17]
	v_mfma_f32_16x16x32_f16 v[78:81], v[134:137], v[90:93], v[78:81]
	v_mfma_f32_16x16x32_f16 v[22:25], v[138:141], v[90:93], v[22:25]
	v_mfma_f32_16x16x32_f16 v[30:33], v[142:145], v[90:93], v[30:33]
	v_mfma_f32_16x16x32_f16 v[74:77], v[134:137], v[94:97], v[74:77]
	v_mfma_f32_16x16x32_f16 v[18:21], v[138:141], v[94:97], v[18:21]
	v_mfma_f32_16x16x32_f16 v[26:29], v[142:145], v[94:97], v[26:29]
	v_mfma_f32_16x16x32_f16 v[70:73], v[134:137], v[98:101], v[70:73]
	v_mfma_f32_16x16x32_f16 v[46:49], v[138:141], v[98:101], v[46:49]
	v_mfma_f32_16x16x32_f16 v[240:243], v[142:145], v[98:101], v[240:243]
	v_mfma_f32_16x16x32_f16 v[66:69], v[134:137], v[102:105], v[66:69]
	v_mfma_f32_16x16x32_f16 v[42:45], v[138:141], v[102:105], v[42:45]
	v_mfma_f32_16x16x32_f16 v[236:239], v[142:145], v[102:105], v[236:239]
	v_mfma_f32_16x16x32_f16 v[62:65], v[134:137], v[106:109], v[62:65]
	v_mfma_f32_16x16x32_f16 v[38:41], v[138:141], v[106:109], v[38:41]
	v_mfma_f32_16x16x32_f16 v[34:37], v[142:145], v[106:109], v[34:37]
	s_waitcnt vmcnt(6) lgkmcnt(0)
	s_barrier
	s_lshl_b32 s26, s17, 2
	s_add_u32 s26, s24, s26
	s_addc_u32 s27, s25, 0
	v_lshlrev_b32_e32 v50, 4, v231
	global_load_dwordx4 v[10:13], v50, s[26:27]
	global_load_dwordx4 v[6:9], v50, s[26:27] offset:64
	global_load_dwordx4 v[2:5], v50, s[26:27] offset:128
	ds_read_b128 v[134:137], v163
	v_mfma_f32_16x16x32_f16 v[82:85], v[146:149], v[110:113], v[82:85]
	ds_read_b128 v[138:141], v163 offset:2048
	v_mfma_f32_16x16x32_f16 v[58:61], v[150:153], v[110:113], v[58:61]
	ds_read_b128 v[142:145], v163 offset:4096
	v_mfma_f32_16x16x32_f16 v[14:17], v[154:157], v[110:113], v[14:17]
	ds_read_b128 v[86:89], v159
	v_mfma_f32_16x16x32_f16 v[78:81], v[146:149], v[114:117], v[78:81]
	ds_read_b128 v[90:93], v159 offset:2048
	v_mfma_f32_16x16x32_f16 v[22:25], v[150:153], v[114:117], v[22:25]
	ds_read_b128 v[94:97], v159 offset:4096
	v_mfma_f32_16x16x32_f16 v[30:33], v[154:157], v[114:117], v[30:33]
	ds_read_b128 v[98:101], v159 offset:6144
	v_mfma_f32_16x16x32_f16 v[74:77], v[146:149], v[118:121], v[74:77]
	ds_read_b128 v[102:105], v159 offset:8192
	v_mfma_f32_16x16x32_f16 v[18:21], v[150:153], v[118:121], v[18:21]
	ds_read_b128 v[106:109], v159 offset:10240
	v_mfma_f32_16x16x32_f16 v[26:29], v[154:157], v[118:121], v[26:29]
	ds_read_b128 v[110:113], v161
	v_mfma_f32_16x16x32_f16 v[70:73], v[146:149], v[122:125], v[70:73]
	ds_read_b128 v[114:117], v161 offset:2048
	v_mfma_f32_16x16x32_f16 v[46:49], v[150:153], v[122:125], v[46:49]
	v_mfma_f32_16x16x32_f16 v[240:243], v[154:157], v[122:125], v[240:243]
	ds_read_b128 v[118:121], v161 offset:4096
	v_mfma_f32_16x16x32_f16 v[66:69], v[146:149], v[126:129], v[66:69]
	ds_read_b128 v[122:125], v161 offset:6144
	v_mfma_f32_16x16x32_f16 v[42:45], v[150:153], v[126:129], v[42:45]
	v_mfma_f32_16x16x32_f16 v[236:239], v[154:157], v[126:129], v[236:239]
	ds_read_b128 v[126:129], v161 offset:8192
	v_mfma_f32_16x16x32_f16 v[62:65], v[146:149], v[130:133], v[62:65]
	v_mfma_f32_16x16x32_f16 v[38:41], v[150:153], v[130:133], v[38:41]
	v_mfma_f32_16x16x32_f16 v[34:37], v[154:157], v[130:133], v[34:37]
	ds_read_b128 v[130:133], v161 offset:10240
	ds_read_b128 v[146:149], v165
	ds_read_b128 v[150:153], v165 offset:2048
	ds_read_b128 v[154:157], v165 offset:4096
	s_waitcnt lgkmcnt(9)
	v_mfma_f32_16x16x32_f16 v[82:85], v[134:137], v[86:89], v[82:85]
	v_mfma_f32_16x16x32_f16 v[58:61], v[138:141], v[86:89], v[58:61]
	v_mfma_f32_16x16x32_f16 v[14:17], v[142:145], v[86:89], v[14:17]
	v_mfma_f32_16x16x32_f16 v[78:81], v[134:137], v[90:93], v[78:81]
	v_mfma_f32_16x16x32_f16 v[22:25], v[138:141], v[90:93], v[22:25]
	v_mfma_f32_16x16x32_f16 v[30:33], v[142:145], v[90:93], v[30:33]
	v_mfma_f32_16x16x32_f16 v[74:77], v[134:137], v[94:97], v[74:77]
	v_mfma_f32_16x16x32_f16 v[18:21], v[138:141], v[94:97], v[18:21]
	v_mfma_f32_16x16x32_f16 v[26:29], v[142:145], v[94:97], v[26:29]
	v_mfma_f32_16x16x32_f16 v[70:73], v[134:137], v[98:101], v[70:73]
	v_mfma_f32_16x16x32_f16 v[46:49], v[138:141], v[98:101], v[46:49]
	v_mfma_f32_16x16x32_f16 v[240:243], v[142:145], v[98:101], v[240:243]
	v_mfma_f32_16x16x32_f16 v[66:69], v[134:137], v[102:105], v[66:69]
	v_mfma_f32_16x16x32_f16 v[42:45], v[138:141], v[102:105], v[42:45]
	v_mfma_f32_16x16x32_f16 v[236:239], v[142:145], v[102:105], v[236:239]
	v_mfma_f32_16x16x32_f16 v[62:65], v[134:137], v[106:109], v[62:65]
	v_mfma_f32_16x16x32_f16 v[38:41], v[138:141], v[106:109], v[38:41]
	v_mfma_f32_16x16x32_f16 v[34:37], v[142:145], v[106:109], v[34:37]
	s_waitcnt vmcnt(3) lgkmcnt(0)
	s_barrier
	ds_read_b128 v[134:137], v162
	v_mfma_f32_16x16x32_f16 v[82:85], v[146:149], v[110:113], v[82:85]
	ds_read_b128 v[138:141], v162 offset:2048
	v_mfma_f32_16x16x32_f16 v[58:61], v[150:153], v[110:113], v[58:61]
	ds_read_b128 v[142:145], v162 offset:4096
	v_mfma_f32_16x16x32_f16 v[14:17], v[154:157], v[110:113], v[14:17]
	ds_read_b128 v[86:89], v158
	v_mfma_f32_16x16x32_f16 v[78:81], v[146:149], v[114:117], v[78:81]
	ds_read_b128 v[90:93], v158 offset:2048
	v_mfma_f32_16x16x32_f16 v[22:25], v[150:153], v[114:117], v[22:25]
	ds_read_b128 v[94:97], v158 offset:4096
	v_mfma_f32_16x16x32_f16 v[30:33], v[154:157], v[114:117], v[30:33]
	ds_read_b128 v[98:101], v158 offset:6144
	v_mfma_f32_16x16x32_f16 v[74:77], v[146:149], v[118:121], v[74:77]
	ds_read_b128 v[102:105], v158 offset:8192
	v_mfma_f32_16x16x32_f16 v[18:21], v[150:153], v[118:121], v[18:21]
	ds_read_b128 v[106:109], v158 offset:10240
	v_mfma_f32_16x16x32_f16 v[26:29], v[154:157], v[118:121], v[26:29]
	ds_read_b128 v[110:113], v160
	v_mfma_f32_16x16x32_f16 v[70:73], v[146:149], v[122:125], v[70:73]
	ds_read_b128 v[114:117], v160 offset:2048
	v_mfma_f32_16x16x32_f16 v[46:49], v[150:153], v[122:125], v[46:49]
	v_mfma_f32_16x16x32_f16 v[240:243], v[154:157], v[122:125], v[240:243]
	ds_read_b128 v[118:121], v160 offset:4096
	v_mfma_f32_16x16x32_f16 v[66:69], v[146:149], v[126:129], v[66:69]
	ds_read_b128 v[122:125], v160 offset:6144
	v_mfma_f32_16x16x32_f16 v[42:45], v[150:153], v[126:129], v[42:45]
	v_mfma_f32_16x16x32_f16 v[236:239], v[154:157], v[126:129], v[236:239]
	ds_read_b128 v[126:129], v160 offset:8192
	v_mfma_f32_16x16x32_f16 v[62:65], v[146:149], v[130:133], v[62:65]
	v_mfma_f32_16x16x32_f16 v[38:41], v[150:153], v[130:133], v[38:41]
	v_mfma_f32_16x16x32_f16 v[34:37], v[154:157], v[130:133], v[34:37]
	ds_read_b128 v[130:133], v160 offset:10240
	ds_read_b128 v[146:149], v164
	ds_read_b128 v[150:153], v164 offset:2048
	ds_read_b128 v[154:157], v164 offset:4096
	s_waitcnt lgkmcnt(9)
	v_mfma_f32_16x16x32_f16 v[82:85], v[134:137], v[86:89], v[82:85]
	v_mfma_f32_16x16x32_f16 v[58:61], v[138:141], v[86:89], v[58:61]
	v_mfma_f32_16x16x32_f16 v[14:17], v[142:145], v[86:89], v[14:17]
	v_mfma_f32_16x16x32_f16 v[78:81], v[134:137], v[90:93], v[78:81]
	v_mfma_f32_16x16x32_f16 v[22:25], v[138:141], v[90:93], v[22:25]
	v_mfma_f32_16x16x32_f16 v[30:33], v[142:145], v[90:93], v[30:33]
	v_mfma_f32_16x16x32_f16 v[74:77], v[134:137], v[94:97], v[74:77]
	v_mfma_f32_16x16x32_f16 v[18:21], v[138:141], v[94:97], v[18:21]
	v_mfma_f32_16x16x32_f16 v[26:29], v[142:145], v[94:97], v[26:29]
	v_mfma_f32_16x16x32_f16 v[70:73], v[134:137], v[98:101], v[70:73]
	v_mfma_f32_16x16x32_f16 v[46:49], v[138:141], v[98:101], v[46:49]
	v_mfma_f32_16x16x32_f16 v[240:243], v[142:145], v[98:101], v[240:243]
	v_mfma_f32_16x16x32_f16 v[66:69], v[134:137], v[102:105], v[66:69]
	v_mfma_f32_16x16x32_f16 v[42:45], v[138:141], v[102:105], v[42:45]
	v_mfma_f32_16x16x32_f16 v[236:239], v[142:145], v[102:105], v[236:239]
	v_mfma_f32_16x16x32_f16 v[62:65], v[134:137], v[106:109], v[62:65]
	v_mfma_f32_16x16x32_f16 v[38:41], v[138:141], v[106:109], v[38:41]
	v_mfma_f32_16x16x32_f16 v[34:37], v[142:145], v[106:109], v[34:37]
	s_waitcnt lgkmcnt(0)
	v_mfma_f32_16x16x32_f16 v[82:85], v[146:149], v[110:113], v[82:85]
	v_mfma_f32_16x16x32_f16 v[58:61], v[150:153], v[110:113], v[58:61]
	v_mfma_f32_16x16x32_f16 v[14:17], v[154:157], v[110:113], v[14:17]
	v_mfma_f32_16x16x32_f16 v[78:81], v[146:149], v[114:117], v[78:81]
	v_mfma_f32_16x16x32_f16 v[22:25], v[150:153], v[114:117], v[22:25]
	v_mfma_f32_16x16x32_f16 v[30:33], v[154:157], v[114:117], v[30:33]
	v_mfma_f32_16x16x32_f16 v[74:77], v[146:149], v[118:121], v[74:77]
	v_mfma_f32_16x16x32_f16 v[18:21], v[150:153], v[118:121], v[18:21]
	v_mfma_f32_16x16x32_f16 v[26:29], v[154:157], v[118:121], v[26:29]
	v_mfma_f32_16x16x32_f16 v[70:73], v[146:149], v[122:125], v[70:73]
	v_mfma_f32_16x16x32_f16 v[46:49], v[150:153], v[122:125], v[46:49]
	v_mfma_f32_16x16x32_f16 v[240:243], v[154:157], v[122:125], v[240:243]
	v_mfma_f32_16x16x32_f16 v[66:69], v[146:149], v[126:129], v[66:69]
	v_mfma_f32_16x16x32_f16 v[42:45], v[150:153], v[126:129], v[42:45]
	v_mfma_f32_16x16x32_f16 v[236:239], v[154:157], v[126:129], v[236:239]
	v_mfma_f32_16x16x32_f16 v[62:65], v[146:149], v[130:133], v[62:65]
	v_mfma_f32_16x16x32_f16 v[38:41], v[150:153], v[130:133], v[38:41]
	v_mfma_f32_16x16x32_f16 v[34:37], v[154:157], v[130:133], v[34:37]
	s_branch .LBB1_76
.Lgemm_N_loop:
	s_waitcnt lgkmcnt(9)
	v_mfma_f32_16x16x32_f16 v[82:85], v[86:89], v[134:137], v[82:85]
	v_mfma_f32_16x16x32_f16 v[58:61], v[86:89], v[138:141], v[58:61]
	v_mfma_f32_16x16x32_f16 v[14:17], v[86:89], v[142:145], v[14:17]
	v_mfma_f32_16x16x32_f16 v[78:81], v[90:93], v[134:137], v[78:81]
	v_mfma_f32_16x16x32_f16 v[22:25], v[90:93], v[138:141], v[22:25]
	v_mfma_f32_16x16x32_f16 v[30:33], v[90:93], v[142:145], v[30:33]
	v_mfma_f32_16x16x32_f16 v[74:77], v[94:97], v[134:137], v[74:77]
	v_mfma_f32_16x16x32_f16 v[18:21], v[94:97], v[138:141], v[18:21]
	v_mfma_f32_16x16x32_f16 v[26:29], v[94:97], v[142:145], v[26:29]
	v_mfma_f32_16x16x32_f16 v[70:73], v[98:101], v[134:137], v[70:73]
	v_mfma_f32_16x16x32_f16 v[46:49], v[98:101], v[138:141], v[46:49]
	v_mfma_f32_16x16x32_f16 v[240:243], v[98:101], v[142:145], v[240:243]
	v_mfma_f32_16x16x32_f16 v[66:69], v[102:105], v[134:137], v[66:69]
	v_mfma_f32_16x16x32_f16 v[42:45], v[102:105], v[138:141], v[42:45]
	v_mfma_f32_16x16x32_f16 v[236:239], v[102:105], v[142:145], v[236:239]
	v_mfma_f32_16x16x32_f16 v[62:65], v[106:109], v[134:137], v[62:65]
	v_mfma_f32_16x16x32_f16 v[38:41], v[106:109], v[138:141], v[38:41]
	v_mfma_f32_16x16x32_f16 v[34:37], v[106:109], v[142:145], v[34:37]
	s_waitcnt vmcnt(6) lgkmcnt(0)
	s_barrier
	s_add_u32 m0, s11, 0x0
	ds_read_b128 v[134:137], v162 offset:49152
	global_load_lds_dwordx4 v[218:219], off
	v_mfma_f32_16x16x32_f16 v[82:85], v[110:113], v[146:149], v[82:85]
	s_add_u32 m0, s11, 0x6000
	ds_read_b128 v[138:141], v162 offset:51200
	global_load_lds_dwordx4 v[220:221], off
	v_mfma_f32_16x16x32_f16 v[58:61], v[110:113], v[150:153], v[58:61]
	s_add_u32 m0, s11, 0x2000
	ds_read_b128 v[142:145], v162 offset:53248
	global_load_lds_dwordx4 v[222:223], off
	v_mfma_f32_16x16x32_f16 v[14:17], v[110:113], v[154:157], v[14:17]
	s_add_u32 m0, s11, 0x8000
	ds_read_b128 v[86:89], v158 offset:49152
	global_load_lds_dwordx4 v[224:225], off
	v_mfma_f32_16x16x32_f16 v[78:81], v[114:117], v[146:149], v[78:81]
	s_add_u32 m0, s11, 0x4000
	ds_read_b128 v[90:93], v158 offset:51200
	global_load_lds_dwordx4 v[226:227], off
	v_mfma_f32_16x16x32_f16 v[22:25], v[114:117], v[150:153], v[22:25]
	s_add_u32 m0, s11, 0xa000
	ds_read_b128 v[94:97], v158 offset:53248
	global_load_lds_dwordx4 v[228:229], off
	v_mfma_f32_16x16x32_f16 v[30:33], v[114:117], v[154:157], v[30:33]
	ds_read_b128 v[98:101], v158 offset:55296
	v_mfma_f32_16x16x32_f16 v[74:77], v[118:121], v[146:149], v[74:77]
	ds_read_b128 v[102:105], v158 offset:57344
	v_mfma_f32_16x16x32_f16 v[18:21], v[118:121], v[150:153], v[18:21]
	ds_read_b128 v[106:109], v158 offset:59392
	v_mfma_f32_16x16x32_f16 v[26:29], v[118:121], v[154:157], v[26:29]
	ds_read_b128 v[110:113], v160 offset:49152
	v_mfma_f32_16x16x32_f16 v[70:73], v[122:125], v[146:149], v[70:73]
	ds_read_b128 v[114:117], v160 offset:51200
	v_mfma_f32_16x16x32_f16 v[46:49], v[122:125], v[150:153], v[46:49]
	v_mfma_f32_16x16x32_f16 v[240:243], v[122:125], v[154:157], v[240:243]
	ds_read_b128 v[118:121], v160 offset:53248
	v_mfma_f32_16x16x32_f16 v[66:69], v[126:129], v[146:149], v[66:69]
	ds_read_b128 v[122:125], v160 offset:55296
	v_mfma_f32_16x16x32_f16 v[42:45], v[126:129], v[150:153], v[42:45]
	v_mfma_f32_16x16x32_f16 v[236:239], v[126:129], v[154:157], v[236:239]
	ds_read_b128 v[126:129], v160 offset:57344
	v_mfma_f32_16x16x32_f16 v[62:65], v[130:133], v[146:149], v[62:65]
	v_mfma_f32_16x16x32_f16 v[38:41], v[130:133], v[150:153], v[38:41]
	v_mfma_f32_16x16x32_f16 v[34:37], v[130:133], v[154:157], v[34:37]
	ds_read_b128 v[130:133], v160 offset:59392
	ds_read_b128 v[146:149], v164 offset:49152
	ds_read_b128 v[150:153], v164 offset:51200
	ds_read_b128 v[154:157], v164 offset:53248
	s_waitcnt lgkmcnt(9)
	v_mfma_f32_16x16x32_f16 v[82:85], v[86:89], v[134:137], v[82:85]
	v_mfma_f32_16x16x32_f16 v[58:61], v[86:89], v[138:141], v[58:61]
	v_mfma_f32_16x16x32_f16 v[14:17], v[86:89], v[142:145], v[14:17]
	v_mfma_f32_16x16x32_f16 v[78:81], v[90:93], v[134:137], v[78:81]
	v_mfma_f32_16x16x32_f16 v[22:25], v[90:93], v[138:141], v[22:25]
	v_mfma_f32_16x16x32_f16 v[30:33], v[90:93], v[142:145], v[30:33]
	v_mfma_f32_16x16x32_f16 v[74:77], v[94:97], v[134:137], v[74:77]
	v_mfma_f32_16x16x32_f16 v[18:21], v[94:97], v[138:141], v[18:21]
	v_mfma_f32_16x16x32_f16 v[26:29], v[94:97], v[142:145], v[26:29]
	v_mfma_f32_16x16x32_f16 v[70:73], v[98:101], v[134:137], v[70:73]
	v_mfma_f32_16x16x32_f16 v[46:49], v[98:101], v[138:141], v[46:49]
	v_mfma_f32_16x16x32_f16 v[240:243], v[98:101], v[142:145], v[240:243]
	v_mfma_f32_16x16x32_f16 v[66:69], v[102:105], v[134:137], v[66:69]
	v_mfma_f32_16x16x32_f16 v[42:45], v[102:105], v[138:141], v[42:45]
	v_mfma_f32_16x16x32_f16 v[236:239], v[102:105], v[142:145], v[236:239]
	v_mfma_f32_16x16x32_f16 v[62:65], v[106:109], v[134:137], v[62:65]
	v_mfma_f32_16x16x32_f16 v[38:41], v[106:109], v[138:141], v[38:41]
	v_mfma_f32_16x16x32_f16 v[34:37], v[106:109], v[142:145], v[34:37]
	s_waitcnt vmcnt(6) lgkmcnt(0)
	s_barrier
	s_add_u32 m0, s11, 0xbf80
	ds_read_b128 v[134:137], v163
	global_load_lds_dwordx4 v[218:219], off offset:128
	v_mfma_f32_16x16x32_f16 v[82:85], v[110:113], v[146:149], v[82:85]
	s_add_u32 m0, s11, 0x11f80
	ds_read_b128 v[138:141], v163 offset:2048
	global_load_lds_dwordx4 v[220:221], off offset:128
	v_mfma_f32_16x16x32_f16 v[58:61], v[110:113], v[150:153], v[58:61]
	s_add_u32 m0, s11, 0xdf80
	ds_read_b128 v[142:145], v163 offset:4096
	global_load_lds_dwordx4 v[222:223], off offset:128
	v_mfma_f32_16x16x32_f16 v[14:17], v[110:113], v[154:157], v[14:17]
	s_add_u32 m0, s11, 0x13f80
	ds_read_b128 v[86:89], v159
	global_load_lds_dwordx4 v[224:225], off offset:128
	v_mfma_f32_16x16x32_f16 v[78:81], v[114:117], v[146:149], v[78:81]
	s_add_u32 m0, s11, 0xff80
	ds_read_b128 v[90:93], v159 offset:2048
	global_load_lds_dwordx4 v[226:227], off offset:128
	v_mfma_f32_16x16x32_f16 v[22:25], v[114:117], v[150:153], v[22:25]
	s_add_u32 m0, s11, 0x15f80
	ds_read_b128 v[94:97], v159 offset:4096
	global_load_lds_dwordx4 v[228:229], off offset:128
	v_mfma_f32_16x16x32_f16 v[30:33], v[114:117], v[154:157], v[30:33]
	ds_read_b128 v[98:101], v159 offset:6144
	v_mfma_f32_16x16x32_f16 v[74:77], v[118:121], v[146:149], v[74:77]
	ds_read_b128 v[102:105], v159 offset:8192
	v_mfma_f32_16x16x32_f16 v[18:21], v[118:121], v[150:153], v[18:21]
	ds_read_b128 v[106:109], v159 offset:10240
	v_mfma_f32_16x16x32_f16 v[26:29], v[118:121], v[154:157], v[26:29]
	ds_read_b128 v[110:113], v161
	v_mfma_f32_16x16x32_f16 v[70:73], v[122:125], v[146:149], v[70:73]
	ds_read_b128 v[114:117], v161 offset:2048
	v_mfma_f32_16x16x32_f16 v[46:49], v[122:125], v[150:153], v[46:49]
	v_mfma_f32_16x16x32_f16 v[240:243], v[122:125], v[154:157], v[240:243]
	ds_read_b128 v[118:121], v161 offset:4096
	v_mfma_f32_16x16x32_f16 v[66:69], v[126:129], v[146:149], v[66:69]
	ds_read_b128 v[122:125], v161 offset:6144
	v_mfma_f32_16x16x32_f16 v[42:45], v[126:129], v[150:153], v[42:45]
	v_mfma_f32_16x16x32_f16 v[236:239], v[126:129], v[154:157], v[236:239]
	ds_read_b128 v[126:129], v161 offset:8192
	v_mfma_f32_16x16x32_f16 v[62:65], v[130:133], v[146:149], v[62:65]
	v_mfma_f32_16x16x32_f16 v[38:41], v[130:133], v[150:153], v[38:41]
	v_mfma_f32_16x16x32_f16 v[34:37], v[130:133], v[154:157], v[34:37]
	ds_read_b128 v[130:133], v161 offset:10240
	ds_read_b128 v[146:149], v165
	ds_read_b128 v[150:153], v165 offset:2048
	ds_read_b128 v[154:157], v165 offset:4096
	s_waitcnt lgkmcnt(9)
	v_mfma_f32_16x16x32_f16 v[82:85], v[86:89], v[134:137], v[82:85]
	v_mfma_f32_16x16x32_f16 v[58:61], v[86:89], v[138:141], v[58:61]
	v_mfma_f32_16x16x32_f16 v[14:17], v[86:89], v[142:145], v[14:17]
	v_mfma_f32_16x16x32_f16 v[78:81], v[90:93], v[134:137], v[78:81]
	v_mfma_f32_16x16x32_f16 v[22:25], v[90:93], v[138:141], v[22:25]
	v_mfma_f32_16x16x32_f16 v[30:33], v[90:93], v[142:145], v[30:33]
	v_mfma_f32_16x16x32_f16 v[74:77], v[94:97], v[134:137], v[74:77]
	v_mfma_f32_16x16x32_f16 v[18:21], v[94:97], v[138:141], v[18:21]
	v_mfma_f32_16x16x32_f16 v[26:29], v[94:97], v[142:145], v[26:29]
	v_mfma_f32_16x16x32_f16 v[70:73], v[98:101], v[134:137], v[70:73]
	v_mfma_f32_16x16x32_f16 v[46:49], v[98:101], v[138:141], v[46:49]
	v_mfma_f32_16x16x32_f16 v[240:243], v[98:101], v[142:145], v[240:243]
	v_mfma_f32_16x16x32_f16 v[66:69], v[102:105], v[134:137], v[66:69]
	v_mfma_f32_16x16x32_f16 v[42:45], v[102:105], v[138:141], v[42:45]
	v_mfma_f32_16x16x32_f16 v[236:239], v[102:105], v[142:145], v[236:239]
	v_mfma_f32_16x16x32_f16 v[62:65], v[106:109], v[134:137], v[62:65]
	v_mfma_f32_16x16x32_f16 v[38:41], v[106:109], v[138:141], v[38:41]
	v_mfma_f32_16x16x32_f16 v[34:37], v[106:109], v[142:145], v[34:37]
	s_waitcnt vmcnt(6) lgkmcnt(0)
	s_barrier
	s_add_u32 m0, s11, 0x17f00
	ds_read_b128 v[134:137], v162
	global_load_lds_dwordx4 v[218:219], off offset:256
	v_mfma_f32_16x16x32_f16 v[82:85], v[110:113], v[146:149], v[82:85]
	s_add_u32 m0, s11, 0x1df00
	ds_read_b128 v[138:141], v162 offset:2048
	global_load_lds_dwordx4 v[220:221], off offset:256
	v_mfma_f32_16x16x32_f16 v[58:61], v[110:113], v[150:153], v[58:61]
	s_add_u32 m0, s11, 0x19f00
	ds_read_b128 v[142:145], v162 offset:4096
	global_load_lds_dwordx4 v[222:223], off offset:256
	v_mfma_f32_16x16x32_f16 v[14:17], v[110:113], v[154:157], v[14:17]
	s_add_u32 m0, s11, 0x1ff00
	ds_read_b128 v[86:89], v158
	global_load_lds_dwordx4 v[224:225], off offset:256
	v_mfma_f32_16x16x32_f16 v[78:81], v[114:117], v[146:149], v[78:81]
	s_add_u32 m0, s11, 0x1bf00
	ds_read_b128 v[90:93], v158 offset:2048
	global_load_lds_dwordx4 v[226:227], off offset:256
	v_mfma_f32_16x16x32_f16 v[22:25], v[114:117], v[150:153], v[22:25]
	s_add_u32 m0, s11, 0x21f00
	ds_read_b128 v[94:97], v158 offset:4096
	global_load_lds_dwordx4 v[228:229], off offset:256
	v_mfma_f32_16x16x32_f16 v[30:33], v[114:117], v[154:157], v[30:33]
	ds_read_b128 v[98:101], v158 offset:6144
	v_mfma_f32_16x16x32_f16 v[74:77], v[118:121], v[146:149], v[74:77]
	ds_read_b128 v[102:105], v158 offset:8192
	v_mfma_f32_16x16x32_f16 v[18:21], v[118:121], v[150:153], v[18:21]
	ds_read_b128 v[106:109], v158 offset:10240
	v_mfma_f32_16x16x32_f16 v[26:29], v[118:121], v[154:157], v[26:29]
	ds_read_b128 v[110:113], v160
	v_mfma_f32_16x16x32_f16 v[70:73], v[122:125], v[146:149], v[70:73]
	ds_read_b128 v[114:117], v160 offset:2048
	v_mfma_f32_16x16x32_f16 v[46:49], v[122:125], v[150:153], v[46:49]
	v_mfma_f32_16x16x32_f16 v[240:243], v[122:125], v[154:157], v[240:243]
	ds_read_b128 v[118:121], v160 offset:4096
	v_mfma_f32_16x16x32_f16 v[66:69], v[126:129], v[146:149], v[66:69]
	ds_read_b128 v[122:125], v160 offset:6144
	v_mfma_f32_16x16x32_f16 v[42:45], v[126:129], v[150:153], v[42:45]
	v_mfma_f32_16x16x32_f16 v[236:239], v[126:129], v[154:157], v[236:239]
	ds_read_b128 v[126:129], v160 offset:8192
	v_mfma_f32_16x16x32_f16 v[62:65], v[130:133], v[146:149], v[62:65]
	v_mfma_f32_16x16x32_f16 v[38:41], v[130:133], v[150:153], v[38:41]
	v_mfma_f32_16x16x32_f16 v[34:37], v[130:133], v[154:157], v[34:37]
	ds_read_b128 v[130:133], v160 offset:10240
	ds_read_b128 v[146:149], v164
	ds_read_b128 v[150:153], v164 offset:2048
	ds_read_b128 v[154:157], v164 offset:4096
	v_lshl_add_u64 v[218:219], v[218:219], 0, s[20:21]
	v_lshl_add_u64 v[222:223], v[222:223], 0, s[20:21]
	v_lshl_add_u64 v[226:227], v[226:227], 0, s[20:21]
	v_lshl_add_u64 v[220:221], v[220:221], 0, s[20:21]
	v_lshl_add_u64 v[224:225], v[224:225], 0, s[20:21]
	v_lshl_add_u64 v[228:229], v[228:229], 0, s[20:21]
	s_sub_u32 s22, s22, 1
	s_cmp_lg_u32 s22, 0
	s_cbranch_scc1 .Lgemm_N_loop
	s_waitcnt lgkmcnt(9)
	v_mfma_f32_16x16x32_f16 v[82:85], v[86:89], v[134:137], v[82:85]
	v_mfma_f32_16x16x32_f16 v[58:61], v[86:89], v[138:141], v[58:61]
	v_mfma_f32_16x16x32_f16 v[14:17], v[86:89], v[142:145], v[14:17]
	v_mfma_f32_16x16x32_f16 v[78:81], v[90:93], v[134:137], v[78:81]
	v_mfma_f32_16x16x32_f16 v[22:25], v[90:93], v[138:141], v[22:25]
	v_mfma_f32_16x16x32_f16 v[30:33], v[90:93], v[142:145], v[30:33]
	v_mfma_f32_16x16x32_f16 v[74:77], v[94:97], v[134:137], v[74:77]
	v_mfma_f32_16x16x32_f16 v[18:21], v[94:97], v[138:141], v[18:21]
	v_mfma_f32_16x16x32_f16 v[26:29], v[94:97], v[142:145], v[26:29]
	v_mfma_f32_16x16x32_f16 v[70:73], v[98:101], v[134:137], v[70:73]
	v_mfma_f32_16x16x32_f16 v[46:49], v[98:101], v[138:141], v[46:49]
	v_mfma_f32_16x16x32_f16 v[240:243], v[98:101], v[142:145], v[240:243]
	v_mfma_f32_16x16x32_f16 v[66:69], v[102:105], v[134:137], v[66:69]
	v_mfma_f32_16x16x32_f16 v[42:45], v[102:105], v[138:141], v[42:45]
	v_mfma_f32_16x16x32_f16 v[236:239], v[102:105], v[142:145], v[236:239]
	v_mfma_f32_16x16x32_f16 v[62:65], v[106:109], v[134:137], v[62:65]
	v_mfma_f32_16x16x32_f16 v[38:41], v[106:109], v[138:141], v[38:41]
	v_mfma_f32_16x16x32_f16 v[34:37], v[106:109], v[142:145], v[34:37]
	s_waitcnt vmcnt(6) lgkmcnt(0)
	s_barrier
	s_add_u32 m0, s11, 0x0
	ds_read_b128 v[134:137], v162 offset:49152
	global_load_lds_dwordx4 v[218:219], off
	v_mfma_f32_16x16x32_f16 v[82:85], v[110:113], v[146:149], v[82:85]
	s_add_u32 m0, s11, 0x6000
	ds_read_b128 v[138:141], v162 offset:51200
	global_load_lds_dwordx4 v[220:221], off
	v_mfma_f32_16x16x32_f16 v[58:61], v[110:113], v[150:153], v[58:61]
	s_add_u32 m0, s11, 0x2000
	ds_read_b128 v[142:145], v162 offset:53248
	global_load_lds_dwordx4 v[222:223], off
	v_mfma_f32_16x16x32_f16 v[14:17], v[110:113], v[154:157], v[14:17]
	s_add_u32 m0, s11, 0x8000
	ds_read_b128 v[86:89], v158 offset:49152
	global_load_lds_dwordx4 v[224:225], off
	v_mfma_f32_16x16x32_f16 v[78:81], v[114:117], v[146:149], v[78:81]
	s_add_u32 m0, s11, 0x4000
	ds_read_b128 v[90:93], v158 offset:51200
	global_load_lds_dwordx4 v[226:227], off
	v_mfma_f32_16x16x32_f16 v[22:25], v[114:117], v[150:153], v[22:25]
	s_add_u32 m0, s11, 0xa000
	ds_read_b128 v[94:97], v158 offset:53248
	global_load_lds_dwordx4 v[228:229], off
	v_mfma_f32_16x16x32_f16 v[30:33], v[114:117], v[154:157], v[30:33]
	ds_read_b128 v[98:101], v158 offset:55296
	v_mfma_f32_16x16x32_f16 v[74:77], v[118:121], v[146:149], v[74:77]
	ds_read_b128 v[102:105], v158 offset:57344
	v_mfma_f32_16x16x32_f16 v[18:21], v[118:121], v[150:153], v[18:21]
	ds_read_b128 v[106:109], v158 offset:59392
	v_mfma_f32_16x16x32_f16 v[26:29], v[118:121], v[154:157], v[26:29]
	ds_read_b128 v[110:113], v160 offset:49152
	v_mfma_f32_16x16x32_f16 v[70:73], v[122:125], v[146:149], v[70:73]
	ds_read_b128 v[114:117], v160 offset:51200
	v_mfma_f32_16x16x32_f16 v[46:49], v[122:125], v[150:153], v[46:49]
	v_mfma_f32_16x16x32_f16 v[240:243], v[122:125], v[154:157], v[240:243]
	ds_read_b128 v[118:121], v160 offset:53248
	v_mfma_f32_16x16x32_f16 v[66:69], v[126:129], v[146:149], v[66:69]
	ds_read_b128 v[122:125], v160 offset:55296
	v_mfma_f32_16x16x32_f16 v[42:45], v[126:129], v[150:153], v[42:45]
	v_mfma_f32_16x16x32_f16 v[236:239], v[126:129], v[154:157], v[236:239]
	ds_read_b128 v[126:129], v160 offset:57344
	v_mfma_f32_16x16x32_f16 v[62:65], v[130:133], v[146:149], v[62:65]
	v_mfma_f32_16x16x32_f16 v[38:41], v[130:133], v[150:153], v[38:41]
	v_mfma_f32_16x16x32_f16 v[34:37], v[130:133], v[154:157], v[34:37]
	ds_read_b128 v[130:133], v160 offset:59392
	ds_read_b128 v[146:149], v164 offset:49152
	ds_read_b128 v[150:153], v164 offset:51200
	ds_read_b128 v[154:157], v164 offset:53248
	s_waitcnt lgkmcnt(9)
	v_mfma_f32_16x16x32_f16 v[82:85], v[86:89], v[134:137], v[82:85]
	v_mfma_f32_16x16x32_f16 v[58:61], v[86:89], v[138:141], v[58:61]
	v_mfma_f32_16x16x32_f16 v[14:17], v[86:89], v[142:145], v[14:17]
	v_mfma_f32_16x16x32_f16 v[78:81], v[90:93], v[134:137], v[78:81]
	v_mfma_f32_16x16x32_f16 v[22:25], v[90:93], v[138:141], v[22:25]
	v_mfma_f32_16x16x32_f16 v[30:33], v[90:93], v[142:145], v[30:33]
	v_mfma_f32_16x16x32_f16 v[74:77], v[94:97], v[134:137], v[74:77]
	v_mfma_f32_16x16x32_f16 v[18:21], v[94:97], v[138:141], v[18:21]
	v_mfma_f32_16x16x32_f16 v[26:29], v[94:97], v[142:145], v[26:29]
	v_mfma_f32_16x16x32_f16 v[70:73], v[98:101], v[134:137], v[70:73]
	v_mfma_f32_16x16x32_f16 v[46:49], v[98:101], v[138:141], v[46:49]
	v_mfma_f32_16x16x32_f16 v[240:243], v[98:101], v[142:145], v[240:243]
	v_mfma_f32_16x16x32_f16 v[66:69], v[102:105], v[134:137], v[66:69]
	v_mfma_f32_16x16x32_f16 v[42:45], v[102:105], v[138:141], v[42:45]
	v_mfma_f32_16x16x32_f16 v[236:239], v[102:105], v[142:145], v[236:239]
	v_mfma_f32_16x16x32_f16 v[62:65], v[106:109], v[134:137], v[62:65]
	v_mfma_f32_16x16x32_f16 v[38:41], v[106:109], v[138:141], v[38:41]
	v_mfma_f32_16x16x32_f16 v[34:37], v[106:109], v[142:145], v[34:37]
	s_waitcnt vmcnt(6) lgkmcnt(0)
	s_barrier
	s_lshl_b32 s26, s17, 2
	s_add_u32 s26, s24, s26
	s_addc_u32 s27, s25, 0
	v_lshlrev_b32_e32 v50, 2, v1
	global_load_dword v234, v50, s[26:27]
	global_load_dword v232, v50, s[26:27] offset:64
	global_load_dword v230, v50, s[26:27] offset:128
	ds_read_b128 v[134:137], v163
	v_mfma_f32_16x16x32_f16 v[82:85], v[110:113], v[146:149], v[82:85]
	ds_read_b128 v[138:141], v163 offset:2048
	v_mfma_f32_16x16x32_f16 v[58:61], v[110:113], v[150:153], v[58:61]
	ds_read_b128 v[142:145], v163 offset:4096
	v_mfma_f32_16x16x32_f16 v[14:17], v[110:113], v[154:157], v[14:17]
	ds_read_b128 v[86:89], v159
	v_mfma_f32_16x16x32_f16 v[78:81], v[114:117], v[146:149], v[78:81]
	ds_read_b128 v[90:93], v159 offset:2048
	v_mfma_f32_16x16x32_f16 v[22:25], v[114:117], v[150:153], v[22:25]
	ds_read_b128 v[94:97], v159 offset:4096
	v_mfma_f32_16x16x32_f16 v[30:33], v[114:117], v[154:157], v[30:33]
	ds_read_b128 v[98:101], v159 offset:6144
	v_mfma_f32_16x16x32_f16 v[74:77], v[118:121], v[146:149], v[74:77]
	ds_read_b128 v[102:105], v159 offset:8192
	v_mfma_f32_16x16x32_f16 v[18:21], v[118:121], v[150:153], v[18:21]
	ds_read_b128 v[106:109], v159 offset:10240
	v_mfma_f32_16x16x32_f16 v[26:29], v[118:121], v[154:157], v[26:29]
	ds_read_b128 v[110:113], v161
	v_mfma_f32_16x16x32_f16 v[70:73], v[122:125], v[146:149], v[70:73]
	ds_read_b128 v[114:117], v161 offset:2048
	v_mfma_f32_16x16x32_f16 v[46:49], v[122:125], v[150:153], v[46:49]
	v_mfma_f32_16x16x32_f16 v[240:243], v[122:125], v[154:157], v[240:243]
	ds_read_b128 v[118:121], v161 offset:4096
	v_mfma_f32_16x16x32_f16 v[66:69], v[126:129], v[146:149], v[66:69]
	ds_read_b128 v[122:125], v161 offset:6144
	v_mfma_f32_16x16x32_f16 v[42:45], v[126:129], v[150:153], v[42:45]
	v_mfma_f32_16x16x32_f16 v[236:239], v[126:129], v[154:157], v[236:239]
	ds_read_b128 v[126:129], v161 offset:8192
	v_mfma_f32_16x16x32_f16 v[62:65], v[130:133], v[146:149], v[62:65]
	v_mfma_f32_16x16x32_f16 v[38:41], v[130:133], v[150:153], v[38:41]
	v_mfma_f32_16x16x32_f16 v[34:37], v[130:133], v[154:157], v[34:37]
	ds_read_b128 v[130:133], v161 offset:10240
	ds_read_b128 v[146:149], v165
	ds_read_b128 v[150:153], v165 offset:2048
	ds_read_b128 v[154:157], v165 offset:4096
	s_waitcnt lgkmcnt(9)
	v_mfma_f32_16x16x32_f16 v[82:85], v[86:89], v[134:137], v[82:85]
	v_mfma_f32_16x16x32_f16 v[58:61], v[86:89], v[138:141], v[58:61]
	v_mfma_f32_16x16x32_f16 v[14:17], v[86:89], v[142:145], v[14:17]
	v_mfma_f32_16x16x32_f16 v[78:81], v[90:93], v[134:137], v[78:81]
	v_mfma_f32_16x16x32_f16 v[22:25], v[90:93], v[138:141], v[22:25]
	v_mfma_f32_16x16x32_f16 v[30:33], v[90:93], v[142:145], v[30:33]
	v_mfma_f32_16x16x32_f16 v[74:77], v[94:97], v[134:137], v[74:77]
	v_mfma_f32_16x16x32_f16 v[18:21], v[94:97], v[138:141], v[18:21]
	v_mfma_f32_16x16x32_f16 v[26:29], v[94:97], v[142:145], v[26:29]
	v_mfma_f32_16x16x32_f16 v[70:73], v[98:101], v[134:137], v[70:73]
	v_mfma_f32_16x16x32_f16 v[46:49], v[98:101], v[138:141], v[46:49]
	v_mfma_f32_16x16x32_f16 v[240:243], v[98:101], v[142:145], v[240:243]
	v_mfma_f32_16x16x32_f16 v[66:69], v[102:105], v[134:137], v[66:69]
	v_mfma_f32_16x16x32_f16 v[42:45], v[102:105], v[138:141], v[42:45]
	v_mfma_f32_16x16x32_f16 v[236:239], v[102:105], v[142:145], v[236:239]
	v_mfma_f32_16x16x32_f16 v[62:65], v[106:109], v[134:137], v[62:65]
	v_mfma_f32_16x16x32_f16 v[38:41], v[106:109], v[138:141], v[38:41]
	v_mfma_f32_16x16x32_f16 v[34:37], v[106:109], v[142:145], v[34:37]
	s_waitcnt vmcnt(3) lgkmcnt(0)
	s_barrier
	ds_read_b128 v[134:137], v162
	v_mfma_f32_16x16x32_f16 v[82:85], v[110:113], v[146:149], v[82:85]
	ds_read_b128 v[138:141], v162 offset:2048
	v_mfma_f32_16x16x32_f16 v[58:61], v[110:113], v[150:153], v[58:61]
	ds_read_b128 v[142:145], v162 offset:4096
	v_mfma_f32_16x16x32_f16 v[14:17], v[110:113], v[154:157], v[14:17]
	ds_read_b128 v[86:89], v158
	v_mfma_f32_16x16x32_f16 v[78:81], v[114:117], v[146:149], v[78:81]
	ds_read_b128 v[90:93], v158 offset:2048
	v_mfma_f32_16x16x32_f16 v[22:25], v[114:117], v[150:153], v[22:25]
	ds_read_b128 v[94:97], v158 offset:4096
	v_mfma_f32_16x16x32_f16 v[30:33], v[114:117], v[154:157], v[30:33]
	ds_read_b128 v[98:101], v158 offset:6144
	v_mfma_f32_16x16x32_f16 v[74:77], v[118:121], v[146:149], v[74:77]
	ds_read_b128 v[102:105], v158 offset:8192
	v_mfma_f32_16x16x32_f16 v[18:21], v[118:121], v[150:153], v[18:21]
	ds_read_b128 v[106:109], v158 offset:10240
	v_mfma_f32_16x16x32_f16 v[26:29], v[118:121], v[154:157], v[26:29]
	ds_read_b128 v[110:113], v160
	v_mfma_f32_16x16x32_f16 v[70:73], v[122:125], v[146:149], v[70:73]
	ds_read_b128 v[114:117], v160 offset:2048
	v_mfma_f32_16x16x32_f16 v[46:49], v[122:125], v[150:153], v[46:49]
	v_mfma_f32_16x16x32_f16 v[240:243], v[122:125], v[154:157], v[240:243]
	ds_read_b128 v[118:121], v160 offset:4096
	v_mfma_f32_16x16x32_f16 v[66:69], v[126:129], v[146:149], v[66:69]
	ds_read_b128 v[122:125], v160 offset:6144
	v_mfma_f32_16x16x32_f16 v[42:45], v[126:129], v[150:153], v[42:45]
	v_mfma_f32_16x16x32_f16 v[236:239], v[126:129], v[154:157], v[236:239]
	ds_read_b128 v[126:129], v160 offset:8192
	v_mfma_f32_16x16x32_f16 v[62:65], v[130:133], v[146:149], v[62:65]
	v_mfma_f32_16x16x32_f16 v[38:41], v[130:133], v[150:153], v[38:41]
	v_mfma_f32_16x16x32_f16 v[34:37], v[130:133], v[154:157], v[34:37]
	ds_read_b128 v[130:133], v160 offset:10240
	ds_read_b128 v[146:149], v164
	ds_read_b128 v[150:153], v164 offset:2048
	ds_read_b128 v[154:157], v164 offset:4096
	s_waitcnt lgkmcnt(9)
	v_mfma_f32_16x16x32_f16 v[82:85], v[86:89], v[134:137], v[82:85]
	v_mfma_f32_16x16x32_f16 v[58:61], v[86:89], v[138:141], v[58:61]
	v_mfma_f32_16x16x32_f16 v[14:17], v[86:89], v[142:145], v[14:17]
	v_mfma_f32_16x16x32_f16 v[78:81], v[90:93], v[134:137], v[78:81]
	v_mfma_f32_16x16x32_f16 v[22:25], v[90:93], v[138:141], v[22:25]
	v_mfma_f32_16x16x32_f16 v[30:33], v[90:93], v[142:145], v[30:33]
	v_mfma_f32_16x16x32_f16 v[74:77], v[94:97], v[134:137], v[74:77]
	v_mfma_f32_16x16x32_f16 v[18:21], v[94:97], v[138:141], v[18:21]
	v_mfma_f32_16x16x32_f16 v[26:29], v[94:97], v[142:145], v[26:29]
	v_mfma_f32_16x16x32_f16 v[70:73], v[98:101], v[134:137], v[70:73]
	v_mfma_f32_16x16x32_f16 v[46:49], v[98:101], v[138:141], v[46:49]
	v_mfma_f32_16x16x32_f16 v[240:243], v[98:101], v[142:145], v[240:243]
	v_mfma_f32_16x16x32_f16 v[66:69], v[102:105], v[134:137], v[66:69]
	v_mfma_f32_16x16x32_f16 v[42:45], v[102:105], v[138:141], v[42:45]
	v_mfma_f32_16x16x32_f16 v[236:239], v[102:105], v[142:145], v[236:239]
	v_mfma_f32_16x16x32_f16 v[62:65], v[106:109], v[134:137], v[62:65]
	v_mfma_f32_16x16x32_f16 v[38:41], v[106:109], v[138:141], v[38:41]
	v_mfma_f32_16x16x32_f16 v[34:37], v[106:109], v[142:145], v[34:37]
	s_waitcnt lgkmcnt(0)
	v_mfma_f32_16x16x32_f16 v[82:85], v[110:113], v[146:149], v[82:85]
	v_mfma_f32_16x16x32_f16 v[58:61], v[110:113], v[150:153], v[58:61]
	v_mfma_f32_16x16x32_f16 v[14:17], v[110:113], v[154:157], v[14:17]
	v_mfma_f32_16x16x32_f16 v[78:81], v[114:117], v[146:149], v[78:81]
	v_mfma_f32_16x16x32_f16 v[22:25], v[114:117], v[150:153], v[22:25]
	v_mfma_f32_16x16x32_f16 v[30:33], v[114:117], v[154:157], v[30:33]
	v_mfma_f32_16x16x32_f16 v[74:77], v[118:121], v[146:149], v[74:77]
	v_mfma_f32_16x16x32_f16 v[18:21], v[118:121], v[150:153], v[18:21]
	v_mfma_f32_16x16x32_f16 v[26:29], v[118:121], v[154:157], v[26:29]
	v_mfma_f32_16x16x32_f16 v[70:73], v[122:125], v[146:149], v[70:73]
	v_mfma_f32_16x16x32_f16 v[46:49], v[122:125], v[150:153], v[46:49]
	v_mfma_f32_16x16x32_f16 v[240:243], v[122:125], v[154:157], v[240:243]
	v_mfma_f32_16x16x32_f16 v[66:69], v[126:129], v[146:149], v[66:69]
	v_mfma_f32_16x16x32_f16 v[42:45], v[126:129], v[150:153], v[42:45]
	v_mfma_f32_16x16x32_f16 v[236:239], v[126:129], v[154:157], v[236:239]
	v_mfma_f32_16x16x32_f16 v[62:65], v[130:133], v[146:149], v[62:65]
	v_mfma_f32_16x16x32_f16 v[38:41], v[130:133], v[150:153], v[38:41]
	v_mfma_f32_16x16x32_f16 v[34:37], v[130:133], v[154:157], v[34:37]
